# GQA loop: hipcc's per-iteration s_setprio 1/0 pair around the fragment reads removed (A/B of the flips)
# speedup vs baseline: 1.0073x; 1.0059x over previous
; __device__ __forceinline__ void phase_s5b_gqa(const Params& P, unsigned char* smraw, int bid, int nb) {
;     ...
;             __builtin_amdgcn_s_setprio(1);
; #pragma unroll
;             for (int kt = 0; kt < 2; ++kt) {
;                 const u32x4 a = *(const u32x4*)&Kb[(kt * 32 + r) * GK8 + h * 32], b2 = *(const u32x4*)&Kb[(kt * 32 + r) * GK8 + h * 32 + 16];
;                 const v8i_t kf = (v8i_t){(int)a.x, (int)a.y, (int)a.z, (int)a.w, (int)b2.x, (int)b2.y, (int)b2.z, (int)b2.w};
;                 s[0][kt] = __builtin_amdgcn_mfma_scale_f32_32x32x64_f8f6f4(kf, qf[0], s[0][kt], 0, 0, 0, one8, 0, one8);
;                 s[1][kt] = __builtin_amdgcn_mfma_scale_f32_32x32x64_f8f6f4(kf, qf[1], s[1][kt], 0, 0, 0, one8, 0, one8);
;             }
;             v8i_t pf[2];
; #pragma unroll
;             for (int qt = 0; qt < 2; ++qt)
; #pragma unroll
;                 for (int kt = 0; kt < 2; ++kt)
; #pragma unroll
;                     for (int g = 0; g < 4; ++g) {
;                         const float p0 = __builtin_amdgcn_exp2f(s[qt][kt][4 * g + 0]), p1 = __builtin_amdgcn_exp2f(s[qt][kt][4 * g + 1]);
;                         const float p2 = __builtin_amdgcn_exp2f(s[qt][kt][4 * g + 2]), p3 = __builtin_amdgcn_exp2f(s[qt][kt][4 * g + 3]);
;                         l2[qt][0] += (hf32x2_t){p0, p1}; l2[qt][1] += (hf32x2_t){p2, p3};
;                         int pk; asm volatile("" : "=v"(pk));
;                         pk = __builtin_amdgcn_cvt_pk_bf8_f32(p0, p1, pk, false);
;                         pk = __builtin_amdgcn_cvt_pk_bf8_f32(p2, p3, pk, true);
;                         pf[qt][kt * 4 + g] = pk;
;                     }
; #pragma unroll
;             for (int dt = 0; dt < 2; ++dt) {
;                 const u32x4 a = *(const u32x4*)&Vb[(dt * 32 + r) * GK8 + h * 32], b2 = *(const u32x4*)&Vb[(dt * 32 + r) * GK8 + h * 32 + 16];
;                 const v8i_t vf = (v8i_t){(int)a.x, (int)a.y, (int)a.z, (int)a.w, (int)b2.x, (int)b2.y, (int)b2.z, (int)b2.w};
.LBB0_1894:
	s_and_b32 s11, s0, 1
	s_mul_i32 s12, s11, 0x1400
	s_nop 0
	v_add_u32_e32 v82, s12, v201
	ds_read_b128 v[98:101], v82 offset:16
	ds_read_b128 v[102:105], v82 offset:32
	ds_read_b128 v[154:157], v82 offset:2576
	ds_read_b128 v[158:161], v82 offset:2592
	ds_read_b128 v[146:149], v82 offset:10256
	ds_read_b128 v[150:153], v82 offset:10272
	ds_read_b128 v[130:133], v82 offset:12816
	ds_read_b128 v[134:137], v82 offset:12832
	s_nop 0
	s_branch .LBB0_1891
